# code placement: three 4-byte pads so the P1/P3/P4 GEMM K-loop heads and both attention loop heads sit at addresses = 0 mod 8 like the baseline (were = 4 mod 8 after earlier edits)
# baseline (speedup 1.0000x reference)
; #define PG8_STAGE(bufoff, gbase, voff) do { _Pragma("unroll") for (int _i = 0; _i < 2; ++_i) \
;         __builtin_amdgcn_global_load_lds((const unsigned*)((const char*)(gbase) + (voff)[_i]), (PG8_LAS unsigned*)(lds + (bufoff) + ldsw + _i * 8192), 16, 0, 0); } while (0)
; #define PG8_LDA(dst, b, h) do { _Pragma("unroll") for (int m = 0; m < 4; ++m) _Pragma("unroll") for (int k = 0; k < 2; ++k) dst[m][k] = *(const PG8_LAS bf16x8*)(lds + PG8_SA(b, h) + aoff + m * 2048 + k * 1024); } while (0)
; #define PG8_LDB(dst, b, h) do { _Pragma("unroll") for (int n = 0; n < 2; ++n) _Pragma("unroll") for (int k = 0; k < 2; ++k) dst[n][k] = *(const PG8_LAS bf16x8*)(lds + PG8_SB(b, h) + boff + n * 2048 + k * 1024); } while (0)
; #define PG8_MMA(ai, bj, At, Bt) do { __builtin_amdgcn_s_setprio(1); _Pragma("unroll") for (int m = 0; m < 4; ++m) _Pragma("unroll") for (int n = 0; n < 2; ++n) _Pragma("unroll") for (int k = 0; k < 2; ++k) \
;         acc[ai][bj][m][n] = __builtin_amdgcn_mfma_f32_16x16x32_bf16(Bt[n][k], At[m][k], acc[ai][bj][m][n], 0, 0, 0); __builtin_amdgcn_s_setprio(0); } while (0)
; #define PG8_WAIT_V(n) asm volatile("s_waitcnt vmcnt(" #n ")" ::: "memory")
; #define PG8_WAIT_L(n) asm volatile("s_waitcnt lgkmcnt(" #n ")" ::: "memory")
; template <class Epi, class Sched, bool ALIGN_EPI = false, bool SP2 = false>
; __device__ __forceinline__ void gemm_phase(PG8_LAS unsigned char* lds, const Gemm g, const Sched& S, const Epi& E) {
;     ...
;             const char* a2 = last ? nA : cA + (size_t)(t + 2) * kstep; const char* b2 = last ? nB : cB + (size_t)(t + 2) * kstep;
;             const char* a3 = a2 + kstep; const char* b3 = b2 + kstep;
;             if (last && has_next) S.a_ready(nxt);
;             if constexpr (Epi::HAS_MID) { if (t != 0 && (t & (Epi::MID_EVERY - 1)) == 0) E.mid(acc, cur, t / Epi::MID_EVERY, wr, wc, fr, fq); }
;             if constexpr (SP2) {
;             PG8_LDB(B0, 0, 0); PG8_LDB(B1, 0, 1); PG8_SCHED; PG8_LDA(At, 0, 0); PG8_STAGE(PG8_SA(1, 1), a1 + hstep, voffA);
;             PG8_WAIT_V(8); PG8_WAIT_L(0); PG8_BAR; PG8_MMA(0, 0, At, B0); PG8_MMA(0, 1, At, B1); PG8_BAR; PG8_SCHED;
;             PG8_LDA(At, 0, 1); PG8_STAGE(PG8_SB(0, 0), b2, voffB); PG8_STAGE(PG8_SB(0, 1), b2 + hstep, voffB); PG8_STAGE(PG8_SA(0, 0), a2, voffA);
;             PG8_WAIT_V(8); PG8_WAIT_L(0); PG8_BAR; PG8_MMA(1, 0, At, B0); PG8_MMA(1, 1, At, B1); PG8_BAR; PG8_SCHED;
.LBB0_152:
	s_nop 0
	s_ashr_i32 s41, s40, 31
	s_lshl_b64 s[42:43], s[40:41], 21
	s_add_u32 s42, s54, s42
	s_addc_u32 s43, s55, s43
	s_and_b64 s[44:45], s[10:11], exec
	s_cselect_b32 s41, s43, s13
	s_cselect_b32 s50, s42, s12
	s_ashr_i32 s39, s38, 31
	s_lshl_b64 s[44:45], s[38:39], 21
	s_add_u32 s44, s56, s44
	s_addc_u32 s45, s57, s45
	s_and_b64 s[48:49], s[10:11], exec
	s_cselect_b32 s39, s45, s47
	s_cselect_b32 s51, s44, s46
	s_add_u32 s12, s12, 0x100080
	s_addc_u32 s13, s13, 0
	s_add_u32 s52, s46, 0x100
	s_addc_u32 s53, s47, 0
	s_mov_b32 s80, -2
	s_add_u32 s46, s12, 0xfff00080
	s_addc_u32 s47, s13, -1
	s_add_i32 s81, 0, 0x10000
	s_cmp_eq_u32 s80, 60
	s_cselect_b32 s49, s41, s47
	s_cselect_b32 s48, s50, s46
	s_cselect_b32 s47, s39, s53
	s_cselect_b32 s46, s51, s52
	s_add_i32 s84, 0, 0x14000
	v_add_u32_e32 v158, s81, v190
	v_add_u32_e32 v174, s84, v190
	s_waitcnt lgkmcnt(0)
	ds_read_b128 v[146:149], v158
	ds_read_b128 v[150:153], v158 offset:1024
	ds_read_b128 v[154:157], v158 offset:2048
	ds_read_b128 v[158:161], v158 offset:3072
	ds_read_b128 v[162:165], v174
	ds_read_b128 v[166:169], v174 offset:1024
	ds_read_b128 v[170:173], v174 offset:2048
	ds_read_b128 v[174:177], v174 offset:3072
	v_lshl_add_u64 v[194:195], s[12:13], 0, v[142:143]
	s_add_i32 m0, s59, 0xc000
	ds_read_b128 v[178:181], v196
	ds_read_b128 v[182:185], v196 offset:1024
	ds_read_b128 v[186:189], v196 offset:2048
	ds_read_b128 v[198:201], v196 offset:3072
	ds_read_b128 v[202:205], v196 offset:4096
	ds_read_b128 v[206:209], v196 offset:5120
	ds_read_b128 v[210:213], v196 offset:6144
	ds_read_b128 v[214:217], v196 offset:7168
	global_load_lds_dwordx4 v[194:195], off
	v_lshl_add_u64 v[194:195], s[12:13], 0, v[144:145]
	s_add_i32 m0, s59, 0xe000
	s_nop 0
	global_load_lds_dwordx4 v[194:195], off
	s_waitcnt vmcnt(8)
	s_waitcnt lgkmcnt(0)
	s_barrier
	s_setprio 1
	s_waitcnt lgkmcnt(0)
	v_mfma_f32_16x16x32_bf16 v[128:131], v[146:149], v[178:181], 0
	v_mfma_f32_16x16x32_bf16 v[124:127], v[154:157], v[178:181], 0
	v_mfma_f32_16x16x32_bf16 v[112:115], v[146:149], v[186:189], 0
	v_mfma_f32_16x16x32_bf16 v[108:111], v[154:157], v[186:189], 0
	v_mfma_f32_16x16x32_bf16 v[96:99], v[146:149], v[202:205], 0
	v_mfma_f32_16x16x32_bf16 v[92:95], v[154:157], v[202:205], 0
	v_mfma_f32_16x16x32_bf16 v[80:83], v[146:149], v[210:213], 0
	v_mfma_f32_16x16x32_bf16 v[76:79], v[154:157], v[210:213], 0
	v_mfma_f32_16x16x32_bf16 v[128:131], v[150:153], v[182:185], v[128:131]
	v_mfma_f32_16x16x32_bf16 v[124:127], v[158:161], v[182:185], v[124:127]
	v_mfma_f32_16x16x32_bf16 v[112:115], v[150:153], v[198:201], v[112:115]
	v_mfma_f32_16x16x32_bf16 v[108:111], v[158:161], v[198:201], v[108:111]
	v_mfma_f32_16x16x32_bf16 v[96:99], v[150:153], v[206:209], v[96:99]
	v_mfma_f32_16x16x32_bf16 v[92:95], v[158:161], v[206:209], v[92:95]
	v_mfma_f32_16x16x32_bf16 v[80:83], v[150:153], v[214:217], v[80:83]
	v_mfma_f32_16x16x32_bf16 v[76:79], v[158:161], v[214:217], v[76:79]
	s_setprio 0
	s_setprio 1
	v_mfma_f32_16x16x32_bf16 v[120:123], v[162:165], v[178:181], 0
	v_mfma_f32_16x16x32_bf16 v[116:119], v[170:173], v[178:181], 0
	v_mfma_f32_16x16x32_bf16 v[104:107], v[162:165], v[186:189], 0
	v_mfma_f32_16x16x32_bf16 v[100:103], v[170:173], v[186:189], 0
	v_mfma_f32_16x16x32_bf16 v[88:91], v[162:165], v[202:205], 0
	v_mfma_f32_16x16x32_bf16 v[84:87], v[170:173], v[202:205], 0
	v_mfma_f32_16x16x32_bf16 v[72:75], v[162:165], v[210:213], 0
	v_mfma_f32_16x16x32_bf16 v[68:71], v[170:173], v[210:213], 0
	v_mfma_f32_16x16x32_bf16 v[120:123], v[166:169], v[182:185], v[120:123]
	v_mfma_f32_16x16x32_bf16 v[116:119], v[174:177], v[182:185], v[116:119]
	v_mfma_f32_16x16x32_bf16 v[104:107], v[166:169], v[198:201], v[104:107]
	v_mfma_f32_16x16x32_bf16 v[100:103], v[174:177], v[198:201], v[100:103]
	v_mfma_f32_16x16x32_bf16 v[88:91], v[166:169], v[206:209], v[88:91]
	v_mfma_f32_16x16x32_bf16 v[84:87], v[174:177], v[206:209], v[84:87]
	v_mfma_f32_16x16x32_bf16 v[72:75], v[166:169], v[214:217], v[72:75]
	v_mfma_f32_16x16x32_bf16 v[68:71], v[174:177], v[214:217], v[68:71]
	s_setprio 0
	s_barrier
; #define PG8_STAGE(bufoff, gbase, voff) do { _Pragma("unroll") for (int _i = 0; _i < 2; ++_i) \
;         __builtin_amdgcn_global_load_lds((const unsigned*)((const char*)(gbase) + (voff)[_i]), (PG8_LAS unsigned*)(lds + (bufoff) + ldsw + _i * 8192), 16, 0, 0); } while (0)
; #define PG8_LDA(dst, b, h) do { _Pragma("unroll") for (int m = 0; m < 4; ++m) _Pragma("unroll") for (int k = 0; k < 2; ++k) dst[m][k] = *(const PG8_LAS bf16x8*)(lds + PG8_SA(b, h) + aoff + m * 2048 + k * 1024); } while (0)
; #define PG8_MMA(ai, bj, At, Bt) do { __builtin_amdgcn_s_setprio(1); _Pragma("unroll") for (int m = 0; m < 4; ++m) _Pragma("unroll") for (int n = 0; n < 2; ++n) _Pragma("unroll") for (int k = 0; k < 2; ++k) \
;         acc[ai][bj][m][n] = __builtin_amdgcn_mfma_f32_16x16x32_bf16(Bt[n][k], At[m][k], acc[ai][bj][m][n], 0, 0, 0); __builtin_amdgcn_s_setprio(0); } while (0)
; #define PG8_WAIT_V(n) asm volatile("s_waitcnt vmcnt(" #n ")" ::: "memory")
; #define PG8_WAIT_L(n) asm volatile("s_waitcnt lgkmcnt(" #n ")" ::: "memory")
; #define PG8_BAR __builtin_amdgcn_s_barrier()
; #define PG8_SCHED __builtin_amdgcn_sched_barrier(0)
; template <class Epi, class Sched, bool ALIGN_EPI = false, bool SP2 = false>
; __device__ __forceinline__ void gemm_phase(PG8_LAS unsigned char* lds, const Gemm g, const Sched& S, const Epi& E) {
;     ...
;             PG8_LDA(At, 0, 1); PG8_STAGE(PG8_SB(0, 0), b2, voffB); PG8_STAGE(PG8_SB(0, 1), b2 + hstep, voffB); PG8_STAGE(PG8_SA(0, 0), a2, voffA);
;             PG8_WAIT_V(8); PG8_WAIT_L(0); PG8_BAR; PG8_MMA(1, 0, At, B0); PG8_MMA(1, 1, At, B1); PG8_BAR; PG8_SCHED;
	s_add_i32 s81, s81, s58
	v_lshl_add_u64 v[194:195], s[46:47], 0, v[2:3]
	s_mov_b32 m0, s81
	ds_read_b128 v[178:181], v196 offset:16384
	ds_read_b128 v[182:185], v196 offset:17408
	ds_read_b128 v[186:189], v196 offset:18432
	ds_read_b128 v[198:201], v196 offset:19456
	ds_read_b128 v[202:205], v196 offset:20480
	ds_read_b128 v[206:209], v196 offset:21504
	ds_read_b128 v[210:213], v196 offset:22528
	ds_read_b128 v[214:217], v196 offset:23552
	global_load_lds_dwordx4 v[194:195], off
	s_add_i32 m0, s81, 0x2000
	s_add_u32 s82, s46, 0x100000
	v_lshl_add_u64 v[222:223], s[46:47], 0, v[132:133]
	s_addc_u32 s83, s47, 0
	s_add_i32 s81, s84, s58
	global_load_lds_dwordx4 v[222:223], off
	v_lshl_add_u64 v[232:233], s[82:83], 0, v[2:3]
	s_mov_b32 m0, s81
	v_lshl_add_u64 v[234:235], s[48:49], 0, v[134:135]
	global_load_lds_dwordx4 v[232:233], off
	v_lshl_add_u64 v[232:233], s[82:83], 0, v[132:133]
	s_add_i32 m0, s81, 0x2000
	s_nop 0
	global_load_lds_dwordx4 v[232:233], off
	v_lshl_add_u64 v[232:233], s[48:49], 0, v[136:137]
	s_mov_b32 m0, s59
	s_nop 0
	global_load_lds_dwordx4 v[232:233], off
	s_mov_b32 m0, s60
	s_nop 0
	global_load_lds_dwordx4 v[234:235], off
	s_waitcnt vmcnt(8)
	s_waitcnt lgkmcnt(0)
	s_barrier
	s_setprio 1
	s_waitcnt lgkmcnt(0)
	v_mfma_f32_16x16x32_bf16 v[64:67], v[146:149], v[178:181], 0
	v_mfma_f32_16x16x32_bf16 v[60:63], v[154:157], v[178:181], 0
	v_mfma_f32_16x16x32_bf16 v[48:51], v[146:149], v[186:189], 0
	v_mfma_f32_16x16x32_bf16 v[44:47], v[154:157], v[186:189], 0
	v_mfma_f32_16x16x32_bf16 v[32:35], v[146:149], v[202:205], 0
	v_mfma_f32_16x16x32_bf16 v[28:31], v[154:157], v[202:205], 0
	v_mfma_f32_16x16x32_bf16 v[16:19], v[146:149], v[210:213], 0
	v_mfma_f32_16x16x32_bf16 v[12:15], v[154:157], v[210:213], 0
	v_mfma_f32_16x16x32_bf16 v[64:67], v[150:153], v[182:185], v[64:67]
	v_mfma_f32_16x16x32_bf16 v[60:63], v[158:161], v[182:185], v[60:63]
	v_mfma_f32_16x16x32_bf16 v[48:51], v[150:153], v[198:201], v[48:51]
	v_mfma_f32_16x16x32_bf16 v[44:47], v[158:161], v[198:201], v[44:47]
	v_mfma_f32_16x16x32_bf16 v[32:35], v[150:153], v[206:209], v[32:35]
	v_mfma_f32_16x16x32_bf16 v[28:31], v[158:161], v[206:209], v[28:31]
	v_mfma_f32_16x16x32_bf16 v[16:19], v[150:153], v[214:217], v[16:19]
	v_mfma_f32_16x16x32_bf16 v[12:15], v[158:161], v[214:217], v[12:15]
	s_setprio 0
	s_setprio 1
	v_mfma_f32_16x16x32_bf16 v[56:59], v[162:165], v[178:181], 0
	v_mfma_f32_16x16x32_bf16 v[52:55], v[170:173], v[178:181], 0
	v_mfma_f32_16x16x32_bf16 v[40:43], v[162:165], v[186:189], 0
	v_mfma_f32_16x16x32_bf16 v[36:39], v[170:173], v[186:189], 0
	v_mfma_f32_16x16x32_bf16 v[24:27], v[162:165], v[202:205], 0
	v_mfma_f32_16x16x32_bf16 v[20:23], v[170:173], v[202:205], 0
	v_mfma_f32_16x16x32_bf16 v[8:11], v[162:165], v[210:213], 0
	v_mfma_f32_16x16x32_bf16 v[4:7], v[170:173], v[210:213], 0
	v_mfma_f32_16x16x32_bf16 v[56:59], v[166:169], v[182:185], v[56:59]
	v_mfma_f32_16x16x32_bf16 v[52:55], v[174:177], v[182:185], v[52:55]
	v_mfma_f32_16x16x32_bf16 v[40:43], v[166:169], v[198:201], v[40:43]
	v_mfma_f32_16x16x32_bf16 v[36:39], v[174:177], v[198:201], v[36:39]
	v_mfma_f32_16x16x32_bf16 v[24:27], v[166:169], v[206:209], v[24:27]
	v_mfma_f32_16x16x32_bf16 v[20:23], v[174:177], v[206:209], v[20:23]
	v_mfma_f32_16x16x32_bf16 v[8:11], v[166:169], v[214:217], v[8:11]
	v_mfma_f32_16x16x32_bf16 v[4:7], v[174:177], v[214:217], v[4:7]
	s_setprio 0
	s_barrier
	s_branch .Lp1_kloop_mid

; __global__ void __launch_bounds__(NWAVES * 64, 2) mega_fwd(Args args) {
;     ...
;             { PHASE_CTX();
;             const bf16_t* PROJ = (const bf16_t*)(ws + WS_PROJ); bf16_t* Y = (bf16_t*)(ws + WS_Y);
;             const bf16_t* mkv = (const bf16_t*)(ws + WS_MKV) + (size_t)l * MEMR * 2048;
;             gu32* qhead = (gu32*)(ws + WS_CTL) + CW_Q + 64 * (l + 2 * rep);
;             const float lam_init = l == 0 ? 0.2f : 0.35550907f;
;             for (;;) {
;                 if (tid == 0) MISC[16] = __hip_atomic_fetch_add(qhead, 1u, RLX_AGENT);
;                 __syncthreads(); const int uq = (int)MISC[16]; __syncthreads();
;                 int lane_u = lane; asm volatile("" : "+v"(lane_u));
.LBB0_423:
	s_nop 0
	v_readlane_b32 s10, v253, 41
	v_readlane_b32 s0, v253, 34
	v_mov_b32_e32 v1, 0x3eb60549
	v_mov_b32_e32 v2, 0x3e4ccccd
	v_readlane_b32 s1, v253, 35
	s_mov_b32 s12, s10
	v_readlane_b32 s11, v253, 42
	v_cndmask_b32_e64 v203, v1, v2, s[0:1]
	v_writelane_b32 v253, s12, 41
	v_mov_b32_e32 v1, v0
	s_mov_b32 s11, s3
	v_writelane_b32 v253, s13, 42
	s_lshl_b64 s[6:7], s[10:11], 22
	v_readfirstlane_b32 s12, v1
	s_lshl_b32 s2, s10, 7
	s_lshl_b32 s0, s10, 8
	s_lshl_b64 s[8:9], s[10:11], 21
	s_lshl_b32 s4, s10, 10
	s_lshl_b64 s[10:11], s[10:11], 19
	v_readlane_b32 s20, v252, 6
	s_ashr_i32 s14, s12, 6
	v_writelane_b32 v253, s10, 54
	v_readlane_b32 s26, v252, 12
	v_readlane_b32 s27, v252, 13
	s_lshl_b32 s13, s14, 14
	v_writelane_b32 v253, s11, 55
	s_mov_b64 s[10:11], s[26:27]
	s_add_i32 s13, s13, 0
	s_add_u32 s18, s10, 0x3c120000
	v_writelane_b32 v253, s13, 56
	s_addc_u32 s19, s11, 0
	v_writelane_b32 v253, s18, 48
	s_mov_b32 s1, s3
	s_mov_b32 s5, s3
	v_writelane_b32 v253, s19, 49
	s_add_u32 s18, s10, 0x59160000
	s_addc_u32 s19, s11, 0
	s_add_u32 s6, s10, s6
	v_writelane_b32 v253, s18, 57
	s_addc_u32 s7, s11, s7
	s_add_u32 s6, s6, 0x3b920000
	v_writelane_b32 v253, s19, 58
	v_writelane_b32 v253, s6, 59
	s_addc_u32 s6, s7, 0
	v_writelane_b32 v253, s6, 60
	s_lshl_b64 s[6:7], s[16:17], 2
	s_add_u32 s6, s10, s6
	s_addc_u32 s7, s11, s7
	s_add_u32 s6, s6, 0x2000
	s_addc_u32 s7, s7, 0
	v_writelane_b32 v253, s6, 61
	v_sub_f32_e32 v205, 1.0, v203
	v_and_b32_e32 v207, 63, v1
	v_writelane_b32 v253, s7, 62
	v_cmp_eq_u32_e64 s[6:7], 0, v1
	v_readlane_b32 s21, v252, 7
	v_readlane_b32 s22, v252, 8
	v_writelane_b32 v253, s6, 63
	v_readlane_b32 s23, v252, 9
	v_readlane_b32 s24, v252, 10
	v_writelane_b32 v254, s7, 0
	s_add_u32 s6, s10, 0x3000
	s_addc_u32 s7, s11, 0
	v_writelane_b32 v254, s6, 1
	v_readlane_b32 s25, v252, 11
	s_nop 0
	v_writelane_b32 v254, s7, 2
	s_lshl_b32 s6, s14, 2
	s_add_i32 s7, s6, 0xffffe000
	s_add_u32 s16, s10, 0x25100000
	v_writelane_b32 v254, s7, 3
	s_addc_u32 s17, s11, 0
	v_writelane_b32 v254, s16, 4
	s_nop 1
	v_writelane_b32 v254, s17, 5
	s_add_u32 s16, s10, 0x21100000
	s_addc_u32 s17, s11, 0
	v_writelane_b32 v254, s16, 6
	s_nop 1
	v_writelane_b32 v254, s17, 7
	s_add_u32 s16, s10, 0x1e100000
	s_addc_u32 s17, s11, 0
	v_writelane_b32 v254, s16, 8
	s_nop 1
	v_writelane_b32 v254, s17, 9
	s_add_u32 s16, s10, 0xe900000
	s_addc_u32 s17, s11, 0
	v_writelane_b32 v254, s16, 10
	s_nop 1
	v_writelane_b32 v254, s17, 11
	v_writelane_b32 v254, s6, 12
	s_addk_i32 s6, 0x7c00
	v_writelane_b32 v254, s6, 13
	s_add_u32 s6, s10, 0x23100000
	s_addc_u32 s7, s11, 0
	v_writelane_b32 v254, s6, 14
	s_nop 1
	v_writelane_b32 v254, s7, 15
	s_add_u32 s6, s10, 0x1f100000
	s_addc_u32 s7, s11, 0
	v_writelane_b32 v254, s6, 16
	s_nop 1
	v_writelane_b32 v254, s7, 17
	s_add_u32 s6, s10, 0x1d100000
	s_addc_u32 s7, s11, 0
	v_writelane_b32 v254, s6, 18
	s_nop 1
	v_writelane_b32 v254, s7, 19
	s_add_u32 s6, s10, 0x100000
	s_addc_u32 s7, s11, 0
	v_writelane_b32 v254, s6, 20
	s_nop 1
	v_writelane_b32 v254, s7, 21
	s_add_u32 s6, s10, 0x59120000
	v_writelane_b32 v254, s6, 22
	s_addc_u32 s6, s11, 0
	v_writelane_b32 v254, s6, 23
	v_writelane_b32 v254, s14, 24
	s_lshl_b32 s6, s14, 5
	v_writelane_b32 v254, s6, 25
	v_readlane_b32 s6, v252, 57
	v_readlane_b32 s7, v252, 58
	s_add_u32 s6, s10, s6
	s_addc_u32 s7, s11, s7
	s_add_u32 s14, s6, 0x5d160000
	s_addc_u32 s15, s7, 0
	v_writelane_b32 v254, s14, 26
	s_add_u32 s6, s6, 0x5d180000
	s_addc_u32 s7, s7, 0
	v_writelane_b32 v254, s15, 27
	v_writelane_b32 v254, s6, 28
	s_nop 1
	v_writelane_b32 v254, s7, 29
	s_add_u32 s6, s10, 0x6f660000
	v_writelane_b32 v254, s6, 30
	s_addc_u32 s6, s11, 0
	v_writelane_b32 v254, s6, 31
	s_and_b32 s6, s12, 0xffffffc0
	v_writelane_b32 v254, s6, 32
	s_add_u32 s6, s10, s8
	s_addc_u32 s7, s11, s9
	s_add_u32 s6, s6, 0x6f160000
	v_writelane_b32 v254, s6, 33
	s_addc_u32 s6, s7, 0
	v_writelane_b32 v254, s6, 34
	s_add_u32 s6, s10, 0x59161800
	s_addc_u32 s7, s11, 0
	v_writelane_b32 v254, s6, 35
	s_nop 1
	v_writelane_b32 v254, s7, 36
	s_add_u32 s6, s10, 0x6f560000
	s_addc_u32 s7, s11, 0
	v_writelane_b32 v254, s6, 37
	s_add_u32 s10, s10, 0x59161000
	s_addc_u32 s11, s11, 0
	v_writelane_b32 v254, s7, 38
	s_lshl_b64 s[6:7], s[2:3], 2
	v_writelane_b32 v254, s6, 39
	s_lshl_b64 s[0:1], s[0:1], 2
	s_nop 0
	v_writelane_b32 v254, s7, 40
	v_writelane_b32 v254, s0, 41
	s_nop 1
	v_writelane_b32 v254, s1, 42
	s_lshl_b64 s[0:1], s[4:5], 2
	v_writelane_b32 v254, s0, 43
	s_nop 1
	v_writelane_b32 v254, s1, 44
	v_writelane_b32 v254, s10, 45
	s_nop 1
	v_writelane_b32 v254, s11, 46
	s_branch .LBB0_427

; template <class Epi, class Sched, bool ALIGN_EPI = false, bool SP2 = false>
; __device__ __forceinline__ void gemm_phase(PG8_LAS unsigned char* lds, const Gemm g, const Sched& S, const Epi& E) {
;     ...
;         const bool has_next = S.next(ui + 1, nxt);
;         const char* nA = has_next ? (const char*)g.A + (size_t)nxt.pm * tstep : cA; const char* nB = has_next ? (const char*)g.Bt + (size_t)nxt.pn * tstep : cB;
;         for (int t = 0; t < nt; t += 2) {
;             const bool last = (t == nt - 2);
;             const char* a1 = cA + (size_t)(t + 1) * kstep;
;             const char* a2 = last ? nA : cA + (size_t)(t + 2) * kstep; const char* b2 = last ? nB : cB + (size_t)(t + 2) * kstep;
;             const char* a3 = a2 + kstep; const char* b3 = b2 + kstep;
;     ...
;         if (!has_next) break;
; #pragma unroll
;         for (int a = 0; a < 2; ++a)
; #pragma unroll
;             for (int b = 0; b < 2; ++b)
; #pragma unroll
;                 for (int m = 0; m < 4; ++m)
; #pragma unroll
;                     for (int n = 0; n < 2; ++n) acc[a][b][m][n] = (f32x4){0.f, 0.f, 0.f, 0.f};
;         cur = nxt; cA = nA; cB = nB; ++ui;
.LBB0_1601:
	s_nop 0
	s_ashr_i32 s17, s16, 31
	s_lshl_b64 s[18:19], s[16:17], 21
	s_add_u32 s18, s34, s18
	s_addc_u32 s19, s35, s19
	s_and_b64 s[20:21], s[0:1], exec
	s_cselect_b32 s17, s19, s23
	s_cselect_b32 s46, s18, s22
	s_ashr_i32 s15, s14, 31
	s_lshl_b64 s[20:21], s[14:15], 21
	s_add_u32 s20, s36, s20
	s_addc_u32 s21, s37, s21
	s_and_b64 s[26:27], s[0:1], exec
	s_cselect_b32 s15, s21, s13
	s_cselect_b32 s47, s20, s12
	s_lshl_b32 s24, s24, 8
	s_ashr_i32 s25, s24, 31
	s_lshl_b32 s26, s2, 8
	v_lshl_add_u64 v[4:5], v[142:143], 0, s[24:25]
	s_ashr_i32 s27, s26, 31
	v_lshl_add_u64 v[6:7], v[144:145], 0, s[26:27]
	v_lshlrev_b64 v[4:5], 12, v[4:5]
	s_add_u32 s28, s22, 0x100080
	v_lshl_add_u64 v[150:151], v[6:7], 0, v[4:5]
	s_addc_u32 s29, s23, 0
	v_mov_b32_e32 v4, v3
	v_mov_b32_e32 v5, v3
	s_add_u32 s25, s12, 0x100
	v_mov_b32_e32 v2, v3
	v_mov_b64_e32 v[8:9], v[4:5]
	v_mov_b64_e32 v[12:13], v[4:5]
	v_mov_b64_e32 v[24:25], v[4:5]
	v_mov_b64_e32 v[28:29], v[4:5]
	v_mov_b64_e32 v[40:41], v[4:5]
	v_mov_b64_e32 v[44:45], v[4:5]
	v_mov_b64_e32 v[56:57], v[4:5]
	v_mov_b64_e32 v[60:61], v[4:5]
	v_mov_b64_e32 v[16:17], v[4:5]
	v_mov_b64_e32 v[20:21], v[4:5]
	v_mov_b64_e32 v[32:33], v[4:5]
	v_mov_b64_e32 v[36:37], v[4:5]
	v_mov_b64_e32 v[48:49], v[4:5]
	v_mov_b64_e32 v[52:53], v[4:5]
	v_mov_b64_e32 v[64:65], v[4:5]
	v_mov_b64_e32 v[68:69], v[4:5]
	v_mov_b64_e32 v[72:73], v[4:5]
	v_mov_b64_e32 v[76:77], v[4:5]
	v_mov_b64_e32 v[88:89], v[4:5]
	v_mov_b64_e32 v[92:93], v[4:5]
	v_mov_b64_e32 v[104:105], v[4:5]
	v_mov_b64_e32 v[108:109], v[4:5]
	v_mov_b64_e32 v[120:121], v[4:5]
	v_mov_b64_e32 v[124:125], v[4:5]
	v_mov_b64_e32 v[80:81], v[4:5]
	v_mov_b64_e32 v[84:85], v[4:5]
	v_mov_b64_e32 v[96:97], v[4:5]
	v_mov_b64_e32 v[100:101], v[4:5]
	v_mov_b64_e32 v[112:113], v[4:5]
	v_mov_b64_e32 v[116:117], v[4:5]
	v_mov_b64_e32 v[128:129], v[4:5]
	v_mov_b64_e32 v[132:133], v[4:5]
	v_lshl_add_u64 v[152:153], s[28:29], 0, v[146:147]
	v_lshl_add_u64 v[154:155], s[28:29], 0, v[148:149]
	s_addc_u32 s27, s13, 0
	s_mov_b32 s48, 0
	s_mov_b64 s[28:29], 0
	v_mov_b64_e32 v[6:7], v[2:3]
	v_mov_b64_e32 v[10:11], v[2:3]
	v_mov_b64_e32 v[22:23], v[2:3]
	v_mov_b64_e32 v[26:27], v[2:3]
	v_mov_b64_e32 v[38:39], v[2:3]
	v_mov_b64_e32 v[42:43], v[2:3]
	v_mov_b64_e32 v[54:55], v[2:3]
	v_mov_b64_e32 v[58:59], v[2:3]
	v_mov_b64_e32 v[14:15], v[2:3]
	v_mov_b64_e32 v[18:19], v[2:3]
	v_mov_b64_e32 v[30:31], v[2:3]
	v_mov_b64_e32 v[34:35], v[2:3]
	v_mov_b64_e32 v[46:47], v[2:3]
	v_mov_b64_e32 v[50:51], v[2:3]
	v_mov_b64_e32 v[62:63], v[2:3]
	v_mov_b64_e32 v[66:67], v[2:3]
	v_mov_b64_e32 v[70:71], v[2:3]
	v_mov_b64_e32 v[74:75], v[2:3]
	v_mov_b64_e32 v[86:87], v[2:3]
	v_mov_b64_e32 v[90:91], v[2:3]
	v_mov_b64_e32 v[102:103], v[2:3]
	v_mov_b64_e32 v[106:107], v[2:3]
	v_mov_b64_e32 v[118:119], v[2:3]
	v_mov_b64_e32 v[122:123], v[2:3]
	v_mov_b64_e32 v[78:79], v[2:3]
	v_mov_b64_e32 v[82:83], v[2:3]
	v_mov_b64_e32 v[94:95], v[2:3]
	v_mov_b64_e32 v[98:99], v[2:3]
	v_mov_b64_e32 v[110:111], v[2:3]
	v_mov_b64_e32 v[114:115], v[2:3]
	v_mov_b64_e32 v[126:127], v[2:3]
	v_mov_b64_e32 v[130:131], v[2:3]
